# baseline (speedup 1.0000x reference)
_Z5k_csrPKiS0_PiS1_PKfS3_S3_S3_PDF16_P15HIP_vector_typeIfLj4EES7_:
	s_cmpk_lt_u32 s2, 0x187
	s_mov_b64 s[4:5], -1
	s_cbranch_scc0 .LBB2_75
	s_mov_b32 s27, s2
	s_load_dwordx8 s[28:35], s[0:1], 0x20
	s_load_dwordx2 s[36:37], s[0:1], 0x40
	v_lshrrev_b32_e32 v56, 6, v0
	v_and_b32_e32 v57, 63, v0
	s_nop 0
	v_readfirstlane_b32 s62, v56
	s_and_b32 s63, s62, 3
	s_lshr_b32 s62, s62, 2
	s_lshl_b32 s62, s62, 6
	v_add_u32_e32 v58, s62, v57
	s_lshl_b32 s62, s2, 8
	v_add_u32_e32 v59, s62, v58
	v_cmp_gt_i32_e32 vcc, 0x186a0, v59
	s_and_saveexec_b64 s[38:39], vcc
	s_cbranch_execz .Ln0b_skip
	v_mul_u32_u24_e32 v60, 40, v59
	s_waitcnt lgkmcnt(0)
	global_load_dwordx4 v[32:35], v60, s[28:29]
	global_load_dwordx4 v[36:39], v60, s[28:29] offset:16
	global_load_dwordx2 v[40:41], v60, s[28:29] offset:32
	s_lshl_b32 s62, s63, 6
	s_add_u32 s30, s30, s62
	s_addc_u32 s31, s31, 0
	s_add_u32 s32, s32, s62
	s_addc_u32 s33, s33, 0
	s_lshl_b32 s62, s63, 9
	s_add_u32 s34, s34, s62
	s_addc_u32 s35, s35, 0
	s_lshl_b32 s62, s63, 5
	v_lshlrev_b32_e32 v60, 7, v59
	v_add_u32_e32 v60, s62, v60
	v_lshlrev_b32_e32 v61, 7, v58
	v_add_u32_e32 v61, s62, v61
	v_add_u32_e32 v61, 0x1740, v61
	v_mov_b32_e32 v44, 0
	v_mov_b32_e32 v45, 0
	v_mov_b32_e32 v46, 0
	v_mov_b32_e32 v47, 0
	v_mov_b32_e32 v48, 0
	v_mov_b32_e32 v49, 0
	v_mov_b32_e32 v50, 0
	v_mov_b32_e32 v51, 0
	s_load_dwordx2 s[40:41], s[30:31], 0x0
	s_load_dwordx2 s[42:43], s[30:31], 0x100
	s_load_dwordx2 s[44:45], s[30:31], 0x200
	s_load_dwordx2 s[46:47], s[30:31], 0x300
	s_load_dwordx2 s[48:49], s[30:31], 0x400
	s_load_dwordx2 s[50:51], s[30:31], 0x500
	s_load_dwordx2 s[52:53], s[30:31], 0x600
	s_load_dwordx2 s[54:55], s[30:31], 0x700
	s_load_dwordx2 s[56:57], s[30:31], 0x800
	s_load_dwordx2 s[58:59], s[30:31], 0x900
	s_load_dwordx2 s[60:61], s[32:33], 0x0
	s_load_dwordx16 s[64:79], s[34:35], 0x0
	s_waitcnt vmcnt(0) lgkmcnt(0)
	v_mov_b32_e32 v42, s60
	v_mov_b32_e32 v43, s61
	v_pk_fma_f32 v[42:43], v[32:33], s[40:41], v[42:43] op_sel_hi:[0,1,1]
	v_pk_fma_f32 v[42:43], v[32:33], s[42:43], v[42:43] op_sel:[1,0,0]
	v_pk_fma_f32 v[42:43], v[34:35], s[44:45], v[42:43] op_sel_hi:[0,1,1]
	v_pk_fma_f32 v[42:43], v[34:35], s[46:47], v[42:43] op_sel:[1,0,0]
	v_pk_fma_f32 v[42:43], v[36:37], s[48:49], v[42:43] op_sel_hi:[0,1,1]
	v_pk_fma_f32 v[42:43], v[36:37], s[50:51], v[42:43] op_sel:[1,0,0]
	v_pk_fma_f32 v[42:43], v[38:39], s[52:53], v[42:43] op_sel_hi:[0,1,1]
	v_pk_fma_f32 v[42:43], v[38:39], s[54:55], v[42:43] op_sel:[1,0,0]
	v_pk_fma_f32 v[42:43], v[40:41], s[56:57], v[42:43] op_sel_hi:[0,1,1]
	v_pk_fma_f32 v[42:43], v[40:41], s[58:59], v[42:43] op_sel:[1,0,0]
	v_max_f32_e32 v42, 0, v42
	v_max_f32_e32 v43, 0, v43
	v_cvt_pk_f16_f32 v52, v42, v43
	v_pk_fma_f32 v[44:45], v[42:43], s[64:65], v[44:45] op_sel_hi:[0,1,1]
	v_pk_fma_f32 v[46:47], v[42:43], s[66:67], v[46:47] op_sel_hi:[0,1,1]
	v_pk_fma_f32 v[48:49], v[42:43], s[68:69], v[48:49] op_sel_hi:[0,1,1]
	v_pk_fma_f32 v[50:51], v[42:43], s[70:71], v[50:51] op_sel_hi:[0,1,1]
	v_pk_fma_f32 v[44:45], v[42:43], s[72:73], v[44:45] op_sel:[1,0,0]
	v_pk_fma_f32 v[46:47], v[42:43], s[74:75], v[46:47] op_sel:[1,0,0]
	v_pk_fma_f32 v[48:49], v[42:43], s[76:77], v[48:49] op_sel:[1,0,0]
	v_pk_fma_f32 v[50:51], v[42:43], s[78:79], v[50:51] op_sel:[1,0,0]
	s_load_dwordx2 s[40:41], s[30:31], 0x8
	s_load_dwordx2 s[42:43], s[30:31], 0x108
	s_load_dwordx2 s[44:45], s[30:31], 0x208
	s_load_dwordx2 s[46:47], s[30:31], 0x308
	s_load_dwordx2 s[48:49], s[30:31], 0x408
	s_load_dwordx2 s[50:51], s[30:31], 0x508
	s_load_dwordx2 s[52:53], s[30:31], 0x608
	s_load_dwordx2 s[54:55], s[30:31], 0x708
	s_load_dwordx2 s[56:57], s[30:31], 0x808
	s_load_dwordx2 s[58:59], s[30:31], 0x908
	s_load_dwordx2 s[60:61], s[32:33], 0x8
	s_load_dwordx16 s[64:79], s[34:35], 0x40
	s_waitcnt lgkmcnt(0)
	v_mov_b32_e32 v42, s60
	v_mov_b32_e32 v43, s61
	v_pk_fma_f32 v[42:43], v[32:33], s[40:41], v[42:43] op_sel_hi:[0,1,1]
	v_pk_fma_f32 v[42:43], v[32:33], s[42:43], v[42:43] op_sel:[1,0,0]
	v_pk_fma_f32 v[42:43], v[34:35], s[44:45], v[42:43] op_sel_hi:[0,1,1]
	v_pk_fma_f32 v[42:43], v[34:35], s[46:47], v[42:43] op_sel:[1,0,0]
	v_pk_fma_f32 v[42:43], v[36:37], s[48:49], v[42:43] op_sel_hi:[0,1,1]
	v_pk_fma_f32 v[42:43], v[36:37], s[50:51], v[42:43] op_sel:[1,0,0]
	v_pk_fma_f32 v[42:43], v[38:39], s[52:53], v[42:43] op_sel_hi:[0,1,1]
	v_pk_fma_f32 v[42:43], v[38:39], s[54:55], v[42:43] op_sel:[1,0,0]
	v_pk_fma_f32 v[42:43], v[40:41], s[56:57], v[42:43] op_sel_hi:[0,1,1]
	v_pk_fma_f32 v[42:43], v[40:41], s[58:59], v[42:43] op_sel:[1,0,0]
	v_max_f32_e32 v42, 0, v42
	v_max_f32_e32 v43, 0, v43
	v_cvt_pk_f16_f32 v53, v42, v43
	v_pk_fma_f32 v[44:45], v[42:43], s[64:65], v[44:45] op_sel_hi:[0,1,1]
	v_pk_fma_f32 v[46:47], v[42:43], s[66:67], v[46:47] op_sel_hi:[0,1,1]
	v_pk_fma_f32 v[48:49], v[42:43], s[68:69], v[48:49] op_sel_hi:[0,1,1]
	v_pk_fma_f32 v[50:51], v[42:43], s[70:71], v[50:51] op_sel_hi:[0,1,1]
	v_pk_fma_f32 v[44:45], v[42:43], s[72:73], v[44:45] op_sel:[1,0,0]
	v_pk_fma_f32 v[46:47], v[42:43], s[74:75], v[46:47] op_sel:[1,0,0]
	v_pk_fma_f32 v[48:49], v[42:43], s[76:77], v[48:49] op_sel:[1,0,0]
	v_pk_fma_f32 v[50:51], v[42:43], s[78:79], v[50:51] op_sel:[1,0,0]
	s_load_dwordx2 s[40:41], s[30:31], 0x10
	s_load_dwordx2 s[42:43], s[30:31], 0x110
	s_load_dwordx2 s[44:45], s[30:31], 0x210
	s_load_dwordx2 s[46:47], s[30:31], 0x310
	s_load_dwordx2 s[48:49], s[30:31], 0x410
	s_load_dwordx2 s[50:51], s[30:31], 0x510
	s_load_dwordx2 s[52:53], s[30:31], 0x610
	s_load_dwordx2 s[54:55], s[30:31], 0x710
	s_load_dwordx2 s[56:57], s[30:31], 0x810
	s_load_dwordx2 s[58:59], s[30:31], 0x910
	s_load_dwordx2 s[60:61], s[32:33], 0x10
	s_load_dwordx16 s[64:79], s[34:35], 0x80
	s_waitcnt lgkmcnt(0)
	v_mov_b32_e32 v42, s60
	v_mov_b32_e32 v43, s61
	v_pk_fma_f32 v[42:43], v[32:33], s[40:41], v[42:43] op_sel_hi:[0,1,1]
	v_pk_fma_f32 v[42:43], v[32:33], s[42:43], v[42:43] op_sel:[1,0,0]
	v_pk_fma_f32 v[42:43], v[34:35], s[44:45], v[42:43] op_sel_hi:[0,1,1]
	v_pk_fma_f32 v[42:43], v[34:35], s[46:47], v[42:43] op_sel:[1,0,0]
	v_pk_fma_f32 v[42:43], v[36:37], s[48:49], v[42:43] op_sel_hi:[0,1,1]
	v_pk_fma_f32 v[42:43], v[36:37], s[50:51], v[42:43] op_sel:[1,0,0]
	v_pk_fma_f32 v[42:43], v[38:39], s[52:53], v[42:43] op_sel_hi:[0,1,1]
	v_pk_fma_f32 v[42:43], v[38:39], s[54:55], v[42:43] op_sel:[1,0,0]
	v_pk_fma_f32 v[42:43], v[40:41], s[56:57], v[42:43] op_sel_hi:[0,1,1]
	v_pk_fma_f32 v[42:43], v[40:41], s[58:59], v[42:43] op_sel:[1,0,0]
	v_max_f32_e32 v42, 0, v42
	v_max_f32_e32 v43, 0, v43
	v_cvt_pk_f16_f32 v54, v42, v43
	v_pk_fma_f32 v[44:45], v[42:43], s[64:65], v[44:45] op_sel_hi:[0,1,1]
	v_pk_fma_f32 v[46:47], v[42:43], s[66:67], v[46:47] op_sel_hi:[0,1,1]
	v_pk_fma_f32 v[48:49], v[42:43], s[68:69], v[48:49] op_sel_hi:[0,1,1]
	v_pk_fma_f32 v[50:51], v[42:43], s[70:71], v[50:51] op_sel_hi:[0,1,1]
	v_pk_fma_f32 v[44:45], v[42:43], s[72:73], v[44:45] op_sel:[1,0,0]
	v_pk_fma_f32 v[46:47], v[42:43], s[74:75], v[46:47] op_sel:[1,0,0]
	v_pk_fma_f32 v[48:49], v[42:43], s[76:77], v[48:49] op_sel:[1,0,0]
	v_pk_fma_f32 v[50:51], v[42:43], s[78:79], v[50:51] op_sel:[1,0,0]
	s_load_dwordx2 s[40:41], s[30:31], 0x18
	s_load_dwordx2 s[42:43], s[30:31], 0x118
	s_load_dwordx2 s[44:45], s[30:31], 0x218
	s_load_dwordx2 s[46:47], s[30:31], 0x318
	s_load_dwordx2 s[48:49], s[30:31], 0x418
	s_load_dwordx2 s[50:51], s[30:31], 0x518
	s_load_dwordx2 s[52:53], s[30:31], 0x618
	s_load_dwordx2 s[54:55], s[30:31], 0x718
	s_load_dwordx2 s[56:57], s[30:31], 0x818
	s_load_dwordx2 s[58:59], s[30:31], 0x918
	s_load_dwordx2 s[60:61], s[32:33], 0x18
	s_load_dwordx16 s[64:79], s[34:35], 0xc0
	s_waitcnt lgkmcnt(0)
	v_mov_b32_e32 v42, s60
	v_mov_b32_e32 v43, s61
	v_pk_fma_f32 v[42:43], v[32:33], s[40:41], v[42:43] op_sel_hi:[0,1,1]
	v_pk_fma_f32 v[42:43], v[32:33], s[42:43], v[42:43] op_sel:[1,0,0]
	v_pk_fma_f32 v[42:43], v[34:35], s[44:45], v[42:43] op_sel_hi:[0,1,1]
	v_pk_fma_f32 v[42:43], v[34:35], s[46:47], v[42:43] op_sel:[1,0,0]
	v_pk_fma_f32 v[42:43], v[36:37], s[48:49], v[42:43] op_sel_hi:[0,1,1]
	v_pk_fma_f32 v[42:43], v[36:37], s[50:51], v[42:43] op_sel:[1,0,0]
	v_pk_fma_f32 v[42:43], v[38:39], s[52:53], v[42:43] op_sel_hi:[0,1,1]
	v_pk_fma_f32 v[42:43], v[38:39], s[54:55], v[42:43] op_sel:[1,0,0]
	v_pk_fma_f32 v[42:43], v[40:41], s[56:57], v[42:43] op_sel_hi:[0,1,1]
	v_pk_fma_f32 v[42:43], v[40:41], s[58:59], v[42:43] op_sel:[1,0,0]
	v_max_f32_e32 v42, 0, v42
	v_max_f32_e32 v43, 0, v43
	v_cvt_pk_f16_f32 v55, v42, v43
	v_pk_fma_f32 v[44:45], v[42:43], s[64:65], v[44:45] op_sel_hi:[0,1,1]
	v_pk_fma_f32 v[46:47], v[42:43], s[66:67], v[46:47] op_sel_hi:[0,1,1]
	v_pk_fma_f32 v[48:49], v[42:43], s[68:69], v[48:49] op_sel_hi:[0,1,1]
	v_pk_fma_f32 v[50:51], v[42:43], s[70:71], v[50:51] op_sel_hi:[0,1,1]
	v_pk_fma_f32 v[44:45], v[42:43], s[72:73], v[44:45] op_sel:[1,0,0]
	v_pk_fma_f32 v[46:47], v[42:43], s[74:75], v[46:47] op_sel:[1,0,0]
	v_pk_fma_f32 v[48:49], v[42:43], s[76:77], v[48:49] op_sel:[1,0,0]
	v_pk_fma_f32 v[50:51], v[42:43], s[78:79], v[50:51] op_sel:[1,0,0]
	global_store_dwordx4 v60, v[52:55], s[36:37] offset:0
	s_load_dwordx2 s[40:41], s[30:31], 0x20
	s_load_dwordx2 s[42:43], s[30:31], 0x120
	s_load_dwordx2 s[44:45], s[30:31], 0x220
	s_load_dwordx2 s[46:47], s[30:31], 0x320
	s_load_dwordx2 s[48:49], s[30:31], 0x420
	s_load_dwordx2 s[50:51], s[30:31], 0x520
	s_load_dwordx2 s[52:53], s[30:31], 0x620
	s_load_dwordx2 s[54:55], s[30:31], 0x720
	s_load_dwordx2 s[56:57], s[30:31], 0x820
	s_load_dwordx2 s[58:59], s[30:31], 0x920
	s_load_dwordx2 s[60:61], s[32:33], 0x20
	s_load_dwordx16 s[64:79], s[34:35], 0x100
	s_waitcnt lgkmcnt(0)
	v_mov_b32_e32 v42, s60
	v_mov_b32_e32 v43, s61
	v_pk_fma_f32 v[42:43], v[32:33], s[40:41], v[42:43] op_sel_hi:[0,1,1]
	v_pk_fma_f32 v[42:43], v[32:33], s[42:43], v[42:43] op_sel:[1,0,0]
	v_pk_fma_f32 v[42:43], v[34:35], s[44:45], v[42:43] op_sel_hi:[0,1,1]
	v_pk_fma_f32 v[42:43], v[34:35], s[46:47], v[42:43] op_sel:[1,0,0]
	v_pk_fma_f32 v[42:43], v[36:37], s[48:49], v[42:43] op_sel_hi:[0,1,1]
	v_pk_fma_f32 v[42:43], v[36:37], s[50:51], v[42:43] op_sel:[1,0,0]
	v_pk_fma_f32 v[42:43], v[38:39], s[52:53], v[42:43] op_sel_hi:[0,1,1]
	v_pk_fma_f32 v[42:43], v[38:39], s[54:55], v[42:43] op_sel:[1,0,0]
	v_pk_fma_f32 v[42:43], v[40:41], s[56:57], v[42:43] op_sel_hi:[0,1,1]
	v_pk_fma_f32 v[42:43], v[40:41], s[58:59], v[42:43] op_sel:[1,0,0]
	v_max_f32_e32 v42, 0, v42
	v_max_f32_e32 v43, 0, v43
	v_cvt_pk_f16_f32 v52, v42, v43
	v_pk_fma_f32 v[44:45], v[42:43], s[64:65], v[44:45] op_sel_hi:[0,1,1]
	v_pk_fma_f32 v[46:47], v[42:43], s[66:67], v[46:47] op_sel_hi:[0,1,1]
	v_pk_fma_f32 v[48:49], v[42:43], s[68:69], v[48:49] op_sel_hi:[0,1,1]
	v_pk_fma_f32 v[50:51], v[42:43], s[70:71], v[50:51] op_sel_hi:[0,1,1]
	v_pk_fma_f32 v[44:45], v[42:43], s[72:73], v[44:45] op_sel:[1,0,0]
	v_pk_fma_f32 v[46:47], v[42:43], s[74:75], v[46:47] op_sel:[1,0,0]
	v_pk_fma_f32 v[48:49], v[42:43], s[76:77], v[48:49] op_sel:[1,0,0]
	v_pk_fma_f32 v[50:51], v[42:43], s[78:79], v[50:51] op_sel:[1,0,0]
	s_load_dwordx2 s[40:41], s[30:31], 0x28
	s_load_dwordx2 s[42:43], s[30:31], 0x128
	s_load_dwordx2 s[44:45], s[30:31], 0x228
	s_load_dwordx2 s[46:47], s[30:31], 0x328
	s_load_dwordx2 s[48:49], s[30:31], 0x428
	s_load_dwordx2 s[50:51], s[30:31], 0x528
	s_load_dwordx2 s[52:53], s[30:31], 0x628
	s_load_dwordx2 s[54:55], s[30:31], 0x728
	s_load_dwordx2 s[56:57], s[30:31], 0x828
	s_load_dwordx2 s[58:59], s[30:31], 0x928
	s_load_dwordx2 s[60:61], s[32:33], 0x28
	s_load_dwordx16 s[64:79], s[34:35], 0x140
	s_waitcnt lgkmcnt(0)
	v_mov_b32_e32 v42, s60
	v_mov_b32_e32 v43, s61
	v_pk_fma_f32 v[42:43], v[32:33], s[40:41], v[42:43] op_sel_hi:[0,1,1]
	v_pk_fma_f32 v[42:43], v[32:33], s[42:43], v[42:43] op_sel:[1,0,0]
	v_pk_fma_f32 v[42:43], v[34:35], s[44:45], v[42:43] op_sel_hi:[0,1,1]
	v_pk_fma_f32 v[42:43], v[34:35], s[46:47], v[42:43] op_sel:[1,0,0]
	v_pk_fma_f32 v[42:43], v[36:37], s[48:49], v[42:43] op_sel_hi:[0,1,1]
	v_pk_fma_f32 v[42:43], v[36:37], s[50:51], v[42:43] op_sel:[1,0,0]
	v_pk_fma_f32 v[42:43], v[38:39], s[52:53], v[42:43] op_sel_hi:[0,1,1]
	v_pk_fma_f32 v[42:43], v[38:39], s[54:55], v[42:43] op_sel:[1,0,0]
	v_pk_fma_f32 v[42:43], v[40:41], s[56:57], v[42:43] op_sel_hi:[0,1,1]
	v_pk_fma_f32 v[42:43], v[40:41], s[58:59], v[42:43] op_sel:[1,0,0]
	v_max_f32_e32 v42, 0, v42
	v_max_f32_e32 v43, 0, v43
	v_cvt_pk_f16_f32 v53, v42, v43
	v_pk_fma_f32 v[44:45], v[42:43], s[64:65], v[44:45] op_sel_hi:[0,1,1]
	v_pk_fma_f32 v[46:47], v[42:43], s[66:67], v[46:47] op_sel_hi:[0,1,1]
	v_pk_fma_f32 v[48:49], v[42:43], s[68:69], v[48:49] op_sel_hi:[0,1,1]
	v_pk_fma_f32 v[50:51], v[42:43], s[70:71], v[50:51] op_sel_hi:[0,1,1]
	v_pk_fma_f32 v[44:45], v[42:43], s[72:73], v[44:45] op_sel:[1,0,0]
	v_pk_fma_f32 v[46:47], v[42:43], s[74:75], v[46:47] op_sel:[1,0,0]
	v_pk_fma_f32 v[48:49], v[42:43], s[76:77], v[48:49] op_sel:[1,0,0]
	v_pk_fma_f32 v[50:51], v[42:43], s[78:79], v[50:51] op_sel:[1,0,0]
	s_load_dwordx2 s[40:41], s[30:31], 0x30
	s_load_dwordx2 s[42:43], s[30:31], 0x130
	s_load_dwordx2 s[44:45], s[30:31], 0x230
	s_load_dwordx2 s[46:47], s[30:31], 0x330
	s_load_dwordx2 s[48:49], s[30:31], 0x430
	s_load_dwordx2 s[50:51], s[30:31], 0x530
	s_load_dwordx2 s[52:53], s[30:31], 0x630
	s_load_dwordx2 s[54:55], s[30:31], 0x730
	s_load_dwordx2 s[56:57], s[30:31], 0x830
	s_load_dwordx2 s[58:59], s[30:31], 0x930
	s_load_dwordx2 s[60:61], s[32:33], 0x30
	s_load_dwordx16 s[64:79], s[34:35], 0x180
	s_waitcnt lgkmcnt(0)
	v_mov_b32_e32 v42, s60
	v_mov_b32_e32 v43, s61
	v_pk_fma_f32 v[42:43], v[32:33], s[40:41], v[42:43] op_sel_hi:[0,1,1]
	v_pk_fma_f32 v[42:43], v[32:33], s[42:43], v[42:43] op_sel:[1,0,0]
	v_pk_fma_f32 v[42:43], v[34:35], s[44:45], v[42:43] op_sel_hi:[0,1,1]
	v_pk_fma_f32 v[42:43], v[34:35], s[46:47], v[42:43] op_sel:[1,0,0]
	v_pk_fma_f32 v[42:43], v[36:37], s[48:49], v[42:43] op_sel_hi:[0,1,1]
	v_pk_fma_f32 v[42:43], v[36:37], s[50:51], v[42:43] op_sel:[1,0,0]
	v_pk_fma_f32 v[42:43], v[38:39], s[52:53], v[42:43] op_sel_hi:[0,1,1]
	v_pk_fma_f32 v[42:43], v[38:39], s[54:55], v[42:43] op_sel:[1,0,0]
	v_pk_fma_f32 v[42:43], v[40:41], s[56:57], v[42:43] op_sel_hi:[0,1,1]
	v_pk_fma_f32 v[42:43], v[40:41], s[58:59], v[42:43] op_sel:[1,0,0]
	v_max_f32_e32 v42, 0, v42
	v_max_f32_e32 v43, 0, v43
	v_cvt_pk_f16_f32 v54, v42, v43
	v_pk_fma_f32 v[44:45], v[42:43], s[64:65], v[44:45] op_sel_hi:[0,1,1]
	v_pk_fma_f32 v[46:47], v[42:43], s[66:67], v[46:47] op_sel_hi:[0,1,1]
	v_pk_fma_f32 v[48:49], v[42:43], s[68:69], v[48:49] op_sel_hi:[0,1,1]
	v_pk_fma_f32 v[50:51], v[42:43], s[70:71], v[50:51] op_sel_hi:[0,1,1]
	v_pk_fma_f32 v[44:45], v[42:43], s[72:73], v[44:45] op_sel:[1,0,0]
	v_pk_fma_f32 v[46:47], v[42:43], s[74:75], v[46:47] op_sel:[1,0,0]
	v_pk_fma_f32 v[48:49], v[42:43], s[76:77], v[48:49] op_sel:[1,0,0]
	v_pk_fma_f32 v[50:51], v[42:43], s[78:79], v[50:51] op_sel:[1,0,0]
	s_load_dwordx2 s[40:41], s[30:31], 0x38
	s_load_dwordx2 s[42:43], s[30:31], 0x138
	s_load_dwordx2 s[44:45], s[30:31], 0x238
	s_load_dwordx2 s[46:47], s[30:31], 0x338
	s_load_dwordx2 s[48:49], s[30:31], 0x438
	s_load_dwordx2 s[50:51], s[30:31], 0x538
	s_load_dwordx2 s[52:53], s[30:31], 0x638
	s_load_dwordx2 s[54:55], s[30:31], 0x738
	s_load_dwordx2 s[56:57], s[30:31], 0x838
	s_load_dwordx2 s[58:59], s[30:31], 0x938
	s_load_dwordx2 s[60:61], s[32:33], 0x38
	s_load_dwordx16 s[64:79], s[34:35], 0x1c0
	s_waitcnt lgkmcnt(0)
	v_mov_b32_e32 v42, s60
	v_mov_b32_e32 v43, s61
	v_pk_fma_f32 v[42:43], v[32:33], s[40:41], v[42:43] op_sel_hi:[0,1,1]
	v_pk_fma_f32 v[42:43], v[32:33], s[42:43], v[42:43] op_sel:[1,0,0]
	v_pk_fma_f32 v[42:43], v[34:35], s[44:45], v[42:43] op_sel_hi:[0,1,1]
	v_pk_fma_f32 v[42:43], v[34:35], s[46:47], v[42:43] op_sel:[1,0,0]
	v_pk_fma_f32 v[42:43], v[36:37], s[48:49], v[42:43] op_sel_hi:[0,1,1]
	v_pk_fma_f32 v[42:43], v[36:37], s[50:51], v[42:43] op_sel:[1,0,0]
	v_pk_fma_f32 v[42:43], v[38:39], s[52:53], v[42:43] op_sel_hi:[0,1,1]
	v_pk_fma_f32 v[42:43], v[38:39], s[54:55], v[42:43] op_sel:[1,0,0]
	v_pk_fma_f32 v[42:43], v[40:41], s[56:57], v[42:43] op_sel_hi:[0,1,1]
	v_pk_fma_f32 v[42:43], v[40:41], s[58:59], v[42:43] op_sel:[1,0,0]
	v_max_f32_e32 v42, 0, v42
	v_max_f32_e32 v43, 0, v43
	v_cvt_pk_f16_f32 v55, v42, v43
	v_pk_fma_f32 v[44:45], v[42:43], s[64:65], v[44:45] op_sel_hi:[0,1,1]
	v_pk_fma_f32 v[46:47], v[42:43], s[66:67], v[46:47] op_sel_hi:[0,1,1]
	v_pk_fma_f32 v[48:49], v[42:43], s[68:69], v[48:49] op_sel_hi:[0,1,1]
	v_pk_fma_f32 v[50:51], v[42:43], s[70:71], v[50:51] op_sel_hi:[0,1,1]
	v_pk_fma_f32 v[44:45], v[42:43], s[72:73], v[44:45] op_sel:[1,0,0]
	v_pk_fma_f32 v[46:47], v[42:43], s[74:75], v[46:47] op_sel:[1,0,0]
	v_pk_fma_f32 v[48:49], v[42:43], s[76:77], v[48:49] op_sel:[1,0,0]
	v_pk_fma_f32 v[50:51], v[42:43], s[78:79], v[50:51] op_sel:[1,0,0]
	global_store_dwordx4 v60, v[52:55], s[36:37] offset:16
	ds_write_b128 v61, v[44:47]
	ds_write_b128 v61, v[48:51] offset:16
.Ln0b_skip:
	s_or_b64 exec, exec, s[38:39]
	s_waitcnt lgkmcnt(0)
	s_load_dwordx4 s[12:15], s[0:1], 0x0
	s_mov_b32 s3, 0
	s_lshl_b64 s[4:5], s[2:3], 2
	s_movk_i32 s3, 0x100
	v_cmp_gt_u32_e32 vcc, s3, v0
	s_waitcnt lgkmcnt(0)
	s_add_u32 s4, s12, s4
	s_addc_u32 s5, s13, s5
	s_load_dwordx2 s[16:17], s[4:5], 0x0
	s_and_saveexec_b64 s[4:5], vcc
	v_lshlrev_b32_e32 v1, 2, v0
	v_mov_b32_e32 v2, 0
	ds_write_b32 v1, v2 offset:4864
	s_or_b64 exec, exec, s[4:5]
	s_waitcnt lgkmcnt(0)
	v_add_u32_e32 v2, s16, v0
	v_cmp_gt_i32_e64 s[4:5], s17, v2
	v_mov_b32_e32 v8, -1
	v_mov_b32_e32 v9, -1
	s_barrier
	s_and_saveexec_b64 s[6:7], s[4:5]
	s_cbranch_execz .LBB2_5
	v_ashrrev_i32_e32 v3, 31, v2
	v_lshl_add_u64 v[4:5], v[2:3], 2, s[14:15]
	global_load_dword v9, v[4:5], off

.LBB2_74:
	s_mov_b64 exec, -1
	s_load_dwordx4 s[28:31], s[0:1], 0x48
	s_lshl_b32 s62, s27, 8
	v_add_u32_e32 v1, s62, v0
	v_cmp_gt_u32_e32 vcc, 0x100, v0
	s_mov_b32 s63, 0x186a0
	v_cmp_gt_i32_e64 s[38:39], s63, v1
	s_and_b64 vcc, vcc, s[38:39]
	s_and_saveexec_b64 s[38:39], vcc
	s_cbranch_execz .Ln0b_fin_done
	v_lshlrev_b32_e32 v2, 3, v1
	v_lshlrev_b32_e32 v3, 4, v1
	v_lshlrev_b32_e32 v4, 7, v0
	v_add_u32_e32 v4, 0x1740, v4
	ds_read_b128 v[32:35], v4 offset:0
	ds_read_b128 v[36:39], v4 offset:16
	ds_read_b128 v[40:43], v4 offset:32
	ds_read_b128 v[44:47], v4 offset:48
	ds_read_b128 v[48:51], v4 offset:64
	ds_read_b128 v[52:55], v4 offset:80
	ds_read_b128 v[56:59], v4 offset:96
	ds_read_b128 v[60:63], v4 offset:112
	s_waitcnt lgkmcnt(0)
	v_pk_add_f32 v[32:33], v[32:33], v[40:41]
	v_pk_add_f32 v[48:49], v[48:49], v[56:57]
	v_pk_add_f32 v[34:35], v[34:35], v[42:43]
	v_pk_add_f32 v[50:51], v[50:51], v[58:59]
	v_pk_add_f32 v[36:37], v[36:37], v[44:45]
	v_pk_add_f32 v[52:53], v[52:53], v[60:61]
	v_pk_add_f32 v[38:39], v[38:39], v[46:47]
	v_pk_add_f32 v[54:55], v[54:55], v[62:63]
	v_pk_add_f32 v[32:33], v[32:33], v[48:49]
	v_pk_add_f32 v[34:35], v[34:35], v[50:51]
	v_pk_add_f32 v[36:37], v[36:37], v[52:53]
	v_pk_add_f32 v[38:39], v[38:39], v[54:55]
	v_cvt_pk_f16_f32 v40, v32, v33
	v_cvt_pk_f16_f32 v41, v34, v35
	global_store_dwordx2 v2, v[40:41], s[28:29]
	global_store_dwordx4 v3, v[36:39], s[30:31]
.Ln0b_fin_done:
	s_or_b64 exec, exec, s[38:39]
	s_mov_b64 s[4:5], 0
.LBB2_75:
	s_and_b64 vcc, exec, s[4:5]
	s_cbranch_vccz .LBB2_84
.LBB2_84:
	s_endpgm

	.amdhsa_kernel _Z5k_csrPKiS0_PiS1_PKfS3_S3_S3_PDF16_P15HIP_vector_typeIfLj4EES7_
		.amdhsa_group_segment_fixed_size 38720
		.amdhsa_private_segment_fixed_size 0
		.amdhsa_kernarg_size 88
		.amdhsa_user_sgpr_count 2
		.amdhsa_user_sgpr_dispatch_ptr 0
		.amdhsa_user_sgpr_queue_ptr 0
		.amdhsa_user_sgpr_kernarg_segment_ptr 1
		.amdhsa_user_sgpr_dispatch_id 0
		.amdhsa_user_sgpr_kernarg_preload_length 0
		.amdhsa_user_sgpr_kernarg_preload_offset 0
		.amdhsa_user_sgpr_private_segment_size 0
		.amdhsa_uses_dynamic_stack 0
		.amdhsa_enable_private_segment 0
		.amdhsa_system_sgpr_workgroup_id_x 1
		.amdhsa_system_sgpr_workgroup_id_y 0
		.amdhsa_system_sgpr_workgroup_id_z 0
		.amdhsa_system_sgpr_workgroup_info 0
		.amdhsa_system_vgpr_workitem_id 0
		.amdhsa_next_free_vgpr 64
		.amdhsa_next_free_sgpr 80
		.amdhsa_accum_offset 64
		.amdhsa_reserve_vcc 1
		.amdhsa_float_round_mode_32 0
		.amdhsa_float_round_mode_16_64 0
		.amdhsa_float_denorm_mode_32 3
		.amdhsa_float_denorm_mode_16_64 3
		.amdhsa_dx10_clamp 1
		.amdhsa_ieee_mode 1
		.amdhsa_fp16_overflow 0
		.amdhsa_tg_split 0
		.amdhsa_exception_fp_ieee_invalid_op 0
		.amdhsa_exception_fp_denorm_src 0
		.amdhsa_exception_fp_ieee_div_zero 0
		.amdhsa_exception_fp_ieee_overflow 0
		.amdhsa_exception_fp_ieee_underflow 0
		.amdhsa_exception_fp_ieee_inexact 0
		.amdhsa_exception_int_div_zero 0
	.end_amdhsa_kernel

_Z7k_layerILi0EEvPKiS1_PKfS3_PKDF16_S3_S5_S5_PDF16_P15HIP_vector_typeIfLj4EES9_S3_S3_S3_S3_S3_S3_PfSA_:
	s_load_dwordx4 s[4:7], s[0:1], 0x20
	s_load_dwordx8 s[8:15], s[0:1], 0x38
	s_load_dwordx8 s[16:23], s[0:1], 0x0
	s_movk_i32 s3, 0x200
	v_readfirstlane_b32 s49, v0
	s_waitcnt lgkmcnt(0)
	s_mov_b64 s[24:25], s[4:5]
	v_cmp_gt_u32_e32 vcc, s3, v0
	v_lshlrev_b32_e32 v6, 2, v0
	s_and_saveexec_b64 s[4:5], vcc
	s_cbranch_execz .LBB5_3
	s_load_dwordx4 s[28:31], s[0:1], 0x58
	v_lshlrev_b32_e32 v83, 2, v0
	s_waitcnt lgkmcnt(0)
	global_load_dword v85, v83, s[28:29]
	global_load_dword v84, v83, s[30:31]
	v_add_u32_e32 v83, 0x6400, v83

.LBB5_11:
	s_lshr_b32 s0, s2, 3
	s_add_i32 s0, s3, s0
	s_lshl_b32 s48, s0, 5
	s_lshl_b32 s50, s33, 3
	s_add_i32 s51, s48, s50
	v_min_u32_e32 v2, 8, v1
	v_add_u32_e32 v2, s51, v2
	v_mov_b32_e32 v3, 0
	v_lshl_add_u64 v[2:3], v[2:3], 2, s[16:17]
	global_load_dword v34, v[2:3], off
	v_and_b32_e32 v35, 15, v0
	s_mov_b32 s27, 0x20000
	s_mov_b32 s30, 0x67c280
	s_and_b32 s29, s19, 0xffff
	v_or_b32_e32 v36, 16, v35
	s_mov_b32 s0, s18
	s_mov_b32 s1, s29
	s_mov_b32 s2, s30
	s_mov_b32 s3, s27
	v_lshrrev_b32_e32 v37, 4, v1
	s_mov_b32 s38, 0xc3500
	s_and_b32 s37, s21, 0xffff
	v_lshlrev_b32_e32 v38, 1, v37
	s_mov_b32 s44, s20
	s_mov_b32 s42, 0x186a00
	s_and_b32 s23, s23, 0xffff
	s_mov_b32 s45, s37
	s_mov_b32 s46, s38
	s_mov_b32 s47, s27
	s_mov_b32 s52, s22
	s_mov_b32 s53, s23
	s_mov_b32 s54, s42
	s_mov_b32 s55, s27
	v_lshlrev_b32_e32 v39, 2, v37
	s_addk_i32 s4, 0x4200
	v_lshlrev_b32_e32 v44, 3, v35
	v_and_b32_e32 v52, 3, v0
	s_and_b32 s25, s25, 0xffff
	s_mov_b32 s31, s27
	s_mov_b32 s39, s27
	s_mov_b32 s36, s20
	s_mov_b32 s43, s27
	v_add_u32_e32 v46, s4, v44
	v_mul_u32_u24_e32 v50, 0x88, v37
	s_mov_b32 s40, s22
	s_mov_b32 s41, s23
	v_mov_b32_e32 v54, 0xff800000
	s_waitcnt vmcnt(0)
	ds_write_b32 v83, v85
	ds_write_b32 v83, v84 offset:1024
	v_readlane_b32 s16, v34, 0
	v_readlane_b32 s17, v34, 1
	s_not_b32 s26, s16
	s_add_i32 s26, s17, s26
	v_min_i32_e32 v2, s26, v35
	v_min_i32_e32 v3, s26, v36
	v_add_lshl_u32 v2, v2, s16, 2
	v_add_lshl_u32 v3, v3, s16, 2
	buffer_load_dword v60, v2, s[0:3], 0 offen
	buffer_load_dword v61, v3, s[0:3], 0 offen
	v_readlane_b32 s26, v34, 2
	s_not_b32 s28, s17
	s_add_i32 s26, s26, s28
	v_min_i32_e32 v2, s26, v35
	v_min_i32_e32 v3, s26, v36
	v_add_lshl_u32 v2, v2, s17, 2
	v_add_lshl_u32 v3, v3, s17, 2
	buffer_load_dword v40, v2, s[0:3], 0 offen
	buffer_load_dword v41, v3, s[0:3], 0 offen
	s_lshl_b32 s16, s51, 4
	v_cmp_gt_u32_e64 s[0:1], 4, v35
	s_lshl_b32 s2, s33, 7
	s_mov_b32 s26, 0xc35000
	s_mov_b32 s28, s18
	s_waitcnt vmcnt(3)
	v_lshl_or_b32 v2, v60, 3, v38
	s_waitcnt vmcnt(2)
	v_lshl_or_b32 v3, v61, 3, v38
	buffer_load_ushort v64, v2, s[44:47], 0 offen
	buffer_load_ushort v63, v3, s[44:47], 0 offen
	buffer_load_dword v62, v39, s[52:55], s16 offen
	v_lshrrev_b32_e32 v2, 2, v0
	v_and_b32_e32 v2, 12, v2
	v_lshl_or_b32 v2, v35, 5, v2
	v_mov_b32_e32 v3, 0x80
	v_cndmask_b32_e64 v2, v3, v2, s[0:1]
	v_lshl_add_u32 v42, v2, 1, s5
	v_and_b32_e32 v2, 0xc0, v6
	v_lshlrev_b32_e32 v3, 1, v35
	v_add3_u32 v43, s5, v2, v3
	v_bfe_u32 v2, v0, 2, 2
	v_or_b32_e32 v2, v39, v2
	v_lshlrev_b32_e32 v3, 3, v0
	v_mul_u32_u24_e32 v2, 0x88, v2
	v_and_b32_e32 v3, 24, v3
	v_add3_u32 v45, s4, v2, v3
	v_cndmask_b32_e64 v2, 0, 32, s[0:1]
	s_add_i32 s16, s2, 0x7040
	v_add_u32_e32 v51, v42, v2
	v_lshlrev_b32_e32 v2, 3, v37
	s_mov_b32 s52, 0
	v_cmp_gt_u32_e64 s[2:3], 16, v1
	v_lshl_or_b32 v47, v35, 2, s16
	v_lshl_add_u32 v48, v1, 2, s16
	v_or_b32_e32 v49, s16, v39
	v_cmp_eq_u32_e64 s[4:5], 2, v52
	v_lshl_or_b32 v53, v35, 7, v2
	s_branch .LBB5_13

_Z7k_layerILi1EEvPKiS1_PKfS3_PKDF16_S3_S5_S5_PDF16_P15HIP_vector_typeIfLj4EES9_S3_S3_S3_S3_S3_S3_PfSA_:
	s_load_dwordx8 s[8:15], s[0:1], 0x38
	s_load_dwordx8 s[16:23], s[0:1], 0x0
	s_load_dwordx2 s[24:25], s[0:1], 0x20
	s_movk_i32 s3, 0x200
	v_readfirstlane_b32 s53, v0
	v_cmp_gt_u32_e32 vcc, s3, v0
	s_and_saveexec_b64 s[4:5], vcc
	s_cbranch_execz .LBB6_3
	s_load_dwordx4 s[28:31], s[0:1], 0x58
	v_lshlrev_b32_e32 v93, 2, v0
	s_waitcnt lgkmcnt(0)
	global_load_dword v95, v93, s[28:29]
	global_load_dword v94, v93, s[30:31]
	v_add_u32_e32 v93, 0x4a00, v93

.LBB6_7:
	s_lshr_b32 s2, s2, 3
	v_and_b32_e32 v78, 31, v0
	v_lshrrev_b32_e32 v6, 3, v0
	s_lshr_b32 s52, s53, 6
	s_add_i32 s2, s3, s2
	v_lshlrev_b32_e32 v2, 5, v78
	v_mov_b32_e32 v3, 0
	v_and_b32_e32 v7, 4, v6
	v_and_b32_e32 v1, 63, v0
	s_lshl_b32 s33, s2, 5
	s_waitcnt lgkmcnt(0)
	v_lshl_add_u64 v[4:5], s[0:1], 0, v[2:3]
	v_lshlrev_b32_e32 v2, 2, v7
	s_lshl_b32 s54, s52, 3
	v_lshl_add_u64 v[4:5], v[4:5], 0, v[2:3]
	s_add_i32 s55, s33, s54
	v_min_u32_e32 v2, 8, v1
	v_add_u32_e32 v2, s55, v2
	v_lshl_add_u64 v[2:3], v[2:3], 2, s[16:17]
	global_load_dword v80, v[2:3], off
	v_and_b32_e32 v81, 15, v0
	s_mov_b32 s27, 0x20000
	s_mov_b32 s30, 0x67c280
	s_and_b32 s29, s19, 0xffff
	v_or_b32_e32 v82, 16, v81
	s_mov_b32 s0, s18
	s_mov_b32 s1, s29
	s_mov_b32 s2, s30
	s_mov_b32 s3, s27
	v_and_b32_e32 v83, 6, v6
	s_mov_b32 s38, 0xc3500
	s_and_b32 s37, s21, 0xffff
	s_mov_b32 s42, 0x186a00
	s_and_b32 s23, s23, 0xffff
	s_mov_b32 s6, s38
	s_mov_b32 s7, s27
	s_mov_b32 s44, s22
	s_mov_b32 s45, s23
	s_mov_b32 s46, s42
	s_mov_b32 s47, s27
	v_lshlrev_b32_e32 v84, 1, v83
	s_lshl_b32 s17, s55, 4
	v_lshlrev_b32_e32 v88, 4, v78
	v_bfe_u32 v90, v0, 4, 2
	v_lshl_or_b32 v89, v7, 1, v88
	v_lshlrev_b32_e32 v7, 4, v81
	s_and_b32 s25, s25, 0xffff
	s_mov_b32 s31, s27
	s_mov_b32 s39, s27
	s_mov_b32 s36, s20
	s_mov_b32 s43, s27
	s_mov_b32 s56, 0
	s_mov_b32 s40, s22
	s_mov_b32 s41, s23
	v_mov_b32_e32 v14, 0xff800000
	s_waitcnt vmcnt(0)
	ds_write_b32 v93, v95
	ds_write_b32 v93, v94 offset:1024
	v_readlane_b32 s4, v80, 0
	v_readlane_b32 s16, v80, 1
	s_not_b32 s5, s4
	s_add_i32 s5, s16, s5
	v_min_i32_e32 v2, s5, v81
	v_min_i32_e32 v3, s5, v82
	v_add_lshl_u32 v2, v2, s4, 2
	v_add_lshl_u32 v3, v3, s4, 2
	buffer_load_dword v21, v2, s[0:3], 0 offen
	buffer_load_dword v20, v3, s[0:3], 0 offen
	v_readlane_b32 s26, v80, 2
	s_not_b32 s28, s16
	s_add_i32 s26, s26, s28
	v_min_i32_e32 v6, s26, v81
	v_min_i32_e32 v8, s26, v82
	v_add_lshl_u32 v6, v6, s16, 2
	s_mov_b32 s4, s20
	s_mov_b32 s5, s37
	global_load_dwordx4 v[2:5], v[4:5], off
	v_add_lshl_u32 v8, v8, s16, 2
	buffer_load_dword v85, v6, s[0:3], 0 offen
	buffer_load_dword v86, v8, s[0:3], 0 offen
	s_lshl_b32 s0, s52, 9
	s_add_i32 s2, s0, 0x4200
	s_lshl_b32 s0, s52, 7
	s_add_i32 s3, s0, 0x5200
	s_mov_b32 s26, 0x30d4000
	s_mov_b32 s28, s18
	v_cmp_gt_u32_e64 s[0:1], 16, v1
	v_lshl_or_b32 v92, v81, 2, s3
	s_waitcnt vmcnt(4)
	v_lshl_or_b32 v6, v21, 3, v83
	s_waitcnt vmcnt(3)
	v_lshl_or_b32 v8, v20, 3, v83
	buffer_load_ushort v24, v6, s[4:7], 0 offen
	buffer_load_ushort v23, v8, s[4:7], 0 offen
	buffer_load_dword v22, v84, s[44:47], s17 offen
	v_lshlrev_b32_e32 v8, 2, v90
	v_or3_b32 v91, s2, v7, v8
	v_lshlrev_b32_e32 v7, 4, v82
	v_bfe_u32 v6, v0, 3, 2
	v_or3_b32 v93, s2, v7, v8
	v_bfe_u32 v7, v0, 5, 1
	v_lshlrev_b32_e32 v8, 2, v6
	v_lshlrev_b32_e32 v79, 2, v7
	v_lshlrev_b32_e32 v87, 4, v7
	v_or_b32_e32 v94, s3, v79
	v_or3_b32 v95, s2, v87, v8
	v_cmp_gt_u32_e64 s[2:3], 8, v78
	v_cmp_eq_u32_e64 s[4:5], 1, v6
	v_cmp_eq_u32_e64 s[6:7], 2, v6
	s_branch .LBB6_10

amdhsa.kernels:
  - .agpr_count:     0
    .args:
      - .actual_access:  read_only
        .address_space:  global
        .offset:         0
        .size:           8
        .value_kind:     global_buffer
      - .actual_access:  write_only
        .address_space:  global
        .offset:         8
        .size:           8
        .value_kind:     global_buffer
      - .actual_access:  read_only
        .address_space:  global
        .offset:         16
        .size:           8
        .value_kind:     global_buffer
      - .actual_access:  read_only
        .address_space:  global
        .offset:         24
        .size:           8
        .value_kind:     global_buffer
      - .actual_access:  read_only
        .address_space:  global
        .offset:         32
        .size:           8
        .value_kind:     global_buffer
      - .actual_access:  read_only
        .address_space:  global
        .offset:         40
        .size:           8
        .value_kind:     global_buffer
      - .actual_access:  read_only
        .address_space:  global
        .offset:         48
        .size:           8
        .value_kind:     global_buffer
      - .actual_access:  read_only
        .address_space:  global
        .offset:         56
        .size:           8
        .value_kind:     global_buffer
      - .actual_access:  read_only
        .address_space:  global
        .offset:         64
        .size:           8
        .value_kind:     global_buffer
      - .actual_access:  read_only
        .address_space:  global
        .offset:         72
        .size:           8
        .value_kind:     global_buffer
      - .actual_access:  read_only
        .address_space:  global
        .offset:         80
        .size:           8
        .value_kind:     global_buffer
      - .actual_access:  write_only
        .address_space:  global
        .offset:         88
        .size:           8
        .value_kind:     global_buffer
      - .actual_access:  write_only
        .address_space:  global
        .offset:         96
        .size:           8
        .value_kind:     global_buffer
      - .actual_access:  write_only
        .address_space:  global
        .offset:         104
        .size:           8
        .value_kind:     global_buffer
      - .actual_access:  write_only
        .address_space:  global
        .offset:         112
        .size:           8
        .value_kind:     global_buffer
      - .actual_access:  write_only
        .address_space:  global
        .offset:         120
        .size:           8
        .value_kind:     global_buffer
    .group_segment_fixed_size: 1564
    .kernarg_segment_align: 8
    .kernarg_segment_size: 128
    .language:       OpenCL C
    .language_version:
      - 2
      - 0
    .max_flat_workgroup_size: 1024
    .name:           _Z6k_pre1PKiPiPKfS3_S3_S3_S3_S3_S3_S3_S3_PDF16_S4_S4_PfS5_
    .private_segment_fixed_size: 0
    .sgpr_count:     22
    .sgpr_spill_count: 0
    .symbol:         _Z6k_pre1PKiPiPKfS3_S3_S3_S3_S3_S3_S3_S3_PDF16_S4_S4_PfS5_.kd
    .uniform_work_group_size: 1
    .uses_dynamic_stack: false
    .vgpr_count:     66
    .vgpr_spill_count: 0
    .wavefront_size: 64
  - .agpr_count:     0
    .args:
      - .actual_access:  read_only
        .address_space:  global
        .offset:         0
        .size:           8
        .value_kind:     global_buffer
      - .actual_access:  read_only
        .address_space:  global
        .offset:         8
        .size:           8
        .value_kind:     global_buffer
      - .actual_access:  read_only
        .address_space:  global
        .offset:         16
        .size:           8
        .value_kind:     global_buffer
      - .actual_access:  read_only
        .address_space:  global
        .offset:         24
        .size:           8
        .value_kind:     global_buffer
      - .actual_access:  write_only
        .address_space:  global
        .offset:         32
        .size:           8
        .value_kind:     global_buffer
      - .actual_access:  write_only
        .address_space:  global
        .offset:         40
        .size:           8
        .value_kind:     global_buffer
    .group_segment_fixed_size: 1632
    .kernarg_segment_align: 8
    .kernarg_segment_size: 48
    .language:       OpenCL C
    .language_version:
      - 2
      - 0
    .max_flat_workgroup_size: 1024
    .name:           _Z9k_scatterPKiS0_S0_S0_PiS1_
    .private_segment_fixed_size: 0
    .sgpr_count:     16
    .sgpr_spill_count: 0
    .symbol:         _Z9k_scatterPKiS0_S0_S0_PiS1_.kd
    .uniform_work_group_size: 1
    .uses_dynamic_stack: false
    .vgpr_count:     50
    .vgpr_spill_count: 0
    .wavefront_size: 64
  - .agpr_count:     0
    .args:
      - .actual_access:  read_only
        .address_space:  global
        .offset:         0
        .size:           8
        .value_kind:     global_buffer
      - .actual_access:  read_only
        .address_space:  global
        .offset:         8
        .size:           8
        .value_kind:     global_buffer
      - .actual_access:  write_only
        .address_space:  global
        .offset:         16
        .size:           8
        .value_kind:     global_buffer
      - .actual_access:  write_only
        .address_space:  global
        .offset:         24
        .size:           8
        .value_kind:     global_buffer
      - .actual_access:  read_only
        .address_space:  global
        .offset:         32
        .size:           8
        .value_kind:     global_buffer
      - .actual_access:  read_only
        .address_space:  global
        .offset:         40
        .size:           8
        .value_kind:     global_buffer
      - .actual_access:  read_only
        .address_space:  global
        .offset:         48
        .size:           8
        .value_kind:     global_buffer
      - .actual_access:  read_only
        .address_space:  global
        .offset:         56
        .size:           8
        .value_kind:     global_buffer
      - .actual_access:  write_only
        .address_space:  global
        .offset:         64
        .size:           8
        .value_kind:     global_buffer
      - .actual_access:  write_only
        .address_space:  global
        .offset:         72
        .size:           8
        .value_kind:     global_buffer
      - .actual_access:  write_only
        .address_space:  global
        .offset:         80
        .size:           8
        .value_kind:     global_buffer
    .group_segment_fixed_size: 38720
    .kernarg_segment_align: 8
    .kernarg_segment_size: 88
    .language:       OpenCL C
    .language_version:
      - 2
      - 0
    .max_flat_workgroup_size: 1024
    .name:           _Z5k_csrPKiS0_PiS1_PKfS3_S3_S3_PDF16_P15HIP_vector_typeIfLj4EES7_
    .private_segment_fixed_size: 0
    .sgpr_count:     86
    .sgpr_spill_count: 0
    .symbol:         _Z5k_csrPKiS0_PiS1_PKfS3_S3_S3_PDF16_P15HIP_vector_typeIfLj4EES7_.kd
    .uniform_work_group_size: 1
    .uses_dynamic_stack: false
    .vgpr_count:     64
    .vgpr_spill_count: 0
    .wavefront_size: 64
  - .agpr_count:     0
    .args:
      - .actual_access:  read_only
        .address_space:  global
        .offset:         0
        .size:           8
        .value_kind:     global_buffer
      - .actual_access:  write_only
        .address_space:  global
        .offset:         8
        .size:           8
        .value_kind:     global_buffer
      - .actual_access:  write_only
        .address_space:  global
        .offset:         16
        .size:           8
        .value_kind:     global_buffer
    .group_segment_fixed_size: 16
    .kernarg_segment_align: 8
    .kernarg_segment_size: 24
    .language:       OpenCL C
    .language_version:
      - 2
      - 0
    .max_flat_workgroup_size: 256
    .name:           _Z6k_pre2PKiPiS1_
    .private_segment_fixed_size: 0
    .sgpr_count:     14
    .sgpr_spill_count: 0
    .symbol:         _Z6k_pre2PKiPiS1_.kd
    .uniform_work_group_size: 1
    .uses_dynamic_stack: false
    .vgpr_count:     14
    .vgpr_spill_count: 0
    .wavefront_size: 64
  - .agpr_count:     0
    .args:
      - .actual_access:  read_only
        .address_space:  global
        .offset:         0
        .size:           8
        .value_kind:     global_buffer
      - .actual_access:  read_only
        .address_space:  global
        .offset:         8
        .size:           8
        .value_kind:     global_buffer
      - .actual_access:  read_only
        .address_space:  global
        .offset:         16
        .size:           8
        .value_kind:     global_buffer
      - .actual_access:  read_only
        .address_space:  global
        .offset:         24
        .size:           8
        .value_kind:     global_buffer
      - .actual_access:  read_only
        .address_space:  global
        .offset:         32
        .size:           8
        .value_kind:     global_buffer
      - .actual_access:  write_only
        .address_space:  global
        .offset:         40
        .size:           8
        .value_kind:     global_buffer
    .group_segment_fixed_size: 1408
    .kernarg_segment_align: 8
    .kernarg_segment_size: 48
    .language:       OpenCL C
    .language_version:
      - 2
      - 0
    .max_flat_workgroup_size: 256
    .name:           _Z7k_finalPKfS0_S0_S0_S0_Pf
    .private_segment_fixed_size: 0
    .sgpr_count:     14
    .sgpr_spill_count: 0
    .symbol:         _Z7k_finalPKfS0_S0_S0_S0_Pf.kd
    .uniform_work_group_size: 1
    .uses_dynamic_stack: false
    .vgpr_count:     29
    .vgpr_spill_count: 0
    .wavefront_size: 64
  - .agpr_count:     0
    .args:
      - .actual_access:  read_only
        .address_space:  global
        .offset:         0
        .size:           8
        .value_kind:     global_buffer
      - .actual_access:  read_only
        .address_space:  global
        .offset:         8
        .size:           8
        .value_kind:     global_buffer
      - .actual_access:  read_only
        .address_space:  global
        .offset:         16
        .size:           8
        .value_kind:     global_buffer
      - .actual_access:  read_only
        .address_space:  global
        .offset:         24
        .size:           8
        .value_kind:     global_buffer
      - .actual_access:  read_only
        .address_space:  global
        .offset:         32
        .size:           8
        .value_kind:     global_buffer
      - .actual_access:  read_only
        .address_space:  global
        .offset:         40
        .size:           8
        .value_kind:     global_buffer
      - .actual_access:  read_only
        .address_space:  global
        .offset:         48
        .size:           8
        .value_kind:     global_buffer
      - .actual_access:  read_only
        .address_space:  global
        .offset:         56
        .size:           8
        .value_kind:     global_buffer
      - .actual_access:  write_only
        .address_space:  global
        .offset:         64
        .size:           8
        .value_kind:     global_buffer
      - .actual_access:  write_only
        .address_space:  global
        .offset:         72
        .size:           8
        .value_kind:     global_buffer
      - .actual_access:  write_only
        .address_space:  global
        .offset:         80
        .size:           8
        .value_kind:     global_buffer
      - .actual_access:  read_only
        .address_space:  global
        .offset:         88
        .size:           8
        .value_kind:     global_buffer
      - .actual_access:  read_only
        .address_space:  global
        .offset:         96
        .size:           8
        .value_kind:     global_buffer
      - .actual_access:  read_only
        .address_space:  global
        .offset:         104
        .size:           8
        .value_kind:     global_buffer
      - .actual_access:  read_only
        .address_space:  global
        .offset:         112
        .size:           8
        .value_kind:     global_buffer
      - .actual_access:  read_only
        .address_space:  global
        .offset:         120
        .size:           8
        .value_kind:     global_buffer
      - .actual_access:  read_only
        .address_space:  global
        .offset:         128
        .size:           8
        .value_kind:     global_buffer
      - .actual_access:  read_only
        .address_space:  global
        .offset:         136
        .size:           8
        .value_kind:     global_buffer
      - .actual_access:  read_only
        .address_space:  global
        .offset:         144
        .size:           8
        .value_kind:     global_buffer
    .group_segment_fixed_size: 29248
    .kernarg_segment_align: 8
    .kernarg_segment_size: 152
    .language:       OpenCL C
    .language_version:
      - 2
      - 0
    .max_flat_workgroup_size: 256
    .name:           _Z7k_layerILi0EEvPKiS1_PKfS3_PKDF16_S3_S5_S5_PDF16_P15HIP_vector_typeIfLj4EES9_S3_S3_S3_S3_S3_S3_PfSA_
    .private_segment_fixed_size: 0
    .sgpr_count:     66
    .sgpr_spill_count: 0
    .symbol:         _Z7k_layerILi0EEvPKiS1_PKfS3_PKDF16_S3_S5_S5_PDF16_P15HIP_vector_typeIfLj4EES9_S3_S3_S3_S3_S3_S3_PfSA_.kd
    .uniform_work_group_size: 1
    .uses_dynamic_stack: false
    .vgpr_count:     86
    .vgpr_spill_count: 0
    .wavefront_size: 64
  - .agpr_count:     0
    .args:
      - .actual_access:  read_only
        .address_space:  global
        .offset:         0
        .size:           8
        .value_kind:     global_buffer
      - .actual_access:  read_only
        .address_space:  global
        .offset:         8
        .size:           8
        .value_kind:     global_buffer
      - .actual_access:  read_only
        .address_space:  global
        .offset:         16
        .size:           8
        .value_kind:     global_buffer
      - .actual_access:  read_only
        .address_space:  global
        .offset:         24
        .size:           8
        .value_kind:     global_buffer
      - .actual_access:  read_only
        .address_space:  global
        .offset:         32
        .size:           8
        .value_kind:     global_buffer
      - .actual_access:  read_only
        .address_space:  global
        .offset:         40
        .size:           8
        .value_kind:     global_buffer
      - .actual_access:  read_only
        .address_space:  global
        .offset:         48
        .size:           8
        .value_kind:     global_buffer
      - .actual_access:  read_only
        .address_space:  global
        .offset:         56
        .size:           8
        .value_kind:     global_buffer
      - .actual_access:  write_only
        .address_space:  global
        .offset:         64
        .size:           8
        .value_kind:     global_buffer
      - .actual_access:  write_only
        .address_space:  global
        .offset:         72
        .size:           8
        .value_kind:     global_buffer
      - .actual_access:  write_only
        .address_space:  global
        .offset:         80
        .size:           8
        .value_kind:     global_buffer
      - .actual_access:  read_only
        .address_space:  global
        .offset:         88
        .size:           8
        .value_kind:     global_buffer
      - .actual_access:  read_only
        .address_space:  global
        .offset:         96
        .size:           8
        .value_kind:     global_buffer
      - .actual_access:  read_only
        .address_space:  global
        .offset:         104
        .size:           8
        .value_kind:     global_buffer
      - .actual_access:  read_only
        .address_space:  global
        .offset:         112
        .size:           8
        .value_kind:     global_buffer
      - .actual_access:  read_only
        .address_space:  global
        .offset:         120
        .size:           8
        .value_kind:     global_buffer
      - .actual_access:  read_only
        .address_space:  global
        .offset:         128
        .size:           8
        .value_kind:     global_buffer
      - .actual_access:  read_only
        .address_space:  global
        .offset:         136
        .size:           8
        .value_kind:     global_buffer
      - .actual_access:  read_only
        .address_space:  global
        .offset:         144
        .size:           8
        .value_kind:     global_buffer
    .group_segment_fixed_size: 21504
    .kernarg_segment_align: 8
    .kernarg_segment_size: 152
    .language:       OpenCL C
    .language_version:
      - 2
      - 0
    .max_flat_workgroup_size: 256
    .name:           _Z7k_layerILi1EEvPKiS1_PKfS3_PKDF16_S3_S5_S5_PDF16_P15HIP_vector_typeIfLj4EES9_S3_S3_S3_S3_S3_S3_PfSA_
    .private_segment_fixed_size: 0
    .sgpr_count:     70
    .sgpr_spill_count: 0
    .symbol:         _Z7k_layerILi1EEvPKiS1_PKfS3_PKDF16_S3_S5_S5_PDF16_P15HIP_vector_typeIfLj4EES9_S3_S3_S3_S3_S3_S3_PfSA_.kd
    .uniform_work_group_size: 1
    .uses_dynamic_stack: false
    .vgpr_count:     96
    .vgpr_spill_count: 0
    .wavefront_size: 64
  - .agpr_count:     0
    .args:
      - .actual_access:  read_only
        .address_space:  global
        .offset:         0
        .size:           8
        .value_kind:     global_buffer
      - .actual_access:  read_only
        .address_space:  global
        .offset:         8
        .size:           8
        .value_kind:     global_buffer
      - .actual_access:  read_only
        .address_space:  global
        .offset:         16
        .size:           8
        .value_kind:     global_buffer
      - .actual_access:  read_only
        .address_space:  global
        .offset:         24
        .size:           8
        .value_kind:     global_buffer
      - .actual_access:  read_only
        .address_space:  global
        .offset:         32
        .size:           8
        .value_kind:     global_buffer
      - .actual_access:  read_only
        .address_space:  global
        .offset:         40
        .size:           8
        .value_kind:     global_buffer
      - .actual_access:  read_only
        .address_space:  global
        .offset:         48
        .size:           8
        .value_kind:     global_buffer
      - .actual_access:  read_only
        .address_space:  global
        .offset:         56
        .size:           8
        .value_kind:     global_buffer
      - .actual_access:  read_only
        .address_space:  global
        .offset:         64
        .size:           8
        .value_kind:     global_buffer
      - .actual_access:  read_only
        .address_space:  global
        .offset:         72
        .size:           8
        .value_kind:     global_buffer
      - .actual_access:  read_only
        .address_space:  global
        .offset:         80
        .size:           8
        .value_kind:     global_buffer
      - .actual_access:  read_only
        .address_space:  global
        .offset:         88
        .size:           8
        .value_kind:     global_buffer
      - .actual_access:  read_only
        .address_space:  global
        .offset:         96
        .size:           8
        .value_kind:     global_buffer
      - .actual_access:  read_only
        .address_space:  global
        .offset:         104
        .size:           8
        .value_kind:     global_buffer
      - .actual_access:  read_only
        .address_space:  global
        .offset:         112
        .size:           8
        .value_kind:     global_buffer
      - .actual_access:  read_only
        .address_space:  global
        .offset:         120
        .size:           8
        .value_kind:     global_buffer
      - .actual_access:  read_only
        .address_space:  global
        .offset:         128
        .size:           8
        .value_kind:     global_buffer
      - .actual_access:  write_only
        .address_space:  global
        .offset:         136
        .size:           8
        .value_kind:     global_buffer
      - .address_space:  global
        .offset:         144
        .size:           8
        .value_kind:     global_buffer
    .group_segment_fixed_size: 19456
    .kernarg_segment_align: 8
    .kernarg_segment_size: 152
    .language:       OpenCL C
    .language_version:
      - 2
      - 0
    .max_flat_workgroup_size: 256
    .name:           _Z7k_layerILi2EEvPKiS1_PKfS3_PKDF16_S3_S5_S5_PDF16_P15HIP_vector_typeIfLj4EES9_S3_S3_S3_S3_S3_S3_PfSA_
    .private_segment_fixed_size: 0
    .sgpr_count:     74
    .sgpr_spill_count: 0
    .symbol:         _Z7k_layerILi2EEvPKiS1_PKfS3_PKDF16_S3_S5_S5_PDF16_P15HIP_vector_typeIfLj4EES9_S3_S3_S3_S3_S3_S3_PfSA_.kd
    .uniform_work_group_size: 1
    .uses_dynamic_stack: false
    .vgpr_count:     110
    .vgpr_spill_count: 0
    .wavefront_size: 64
